# static s_setprio 1 for waves 4-7 during GEMM phases only (per-block flips removed)
# baseline (speedup 1.0000x reference)
; #define PG8_LAS __attribute__((address_space(3)))
; template <class Epi, class Sched, bool ALIGN_EPI = false>
; __device__ __forceinline__ void gemm_phase(PG8_LAS unsigned char* lds, const Gemm g, const Sched& S, const Epi& E) {
;     const int tid = threadIdx.x, wid = __builtin_amdgcn_readfirstlane(tid >> 6), lane = tid & 63, wr = wid >> 2, wc = wid & 3, fr = lane & 15, fq = lane >> 4;
.LBB0_237:
	s_cmp_lt_u32 s33, 4
	s_cbranch_scc1 .Lprio_skip_1
	s_setprio 1

; template <int PASS> ...
;     ...
;     const int tokbase = p * CPP * CHK;
;     const unsigned qkoff = (unsigned)((tid >> 5) * KD + h * DKH + (tid & 31) * 8) * 2u, voff = (unsigned)((tid >> 4) * VD + h * DVH + s * 128 + (tid & 15) * 8) * 2u;
;     Stage st0, st1;
;     issue_loads<NQ>(st0, QP, KP, VB, BC, tokbase, h, s, tid, qkoff, voff);
;     __syncthreads();
;     if (PASS == 2 && p > 0) {
;         LAS int* cw = (LAS int*)(lds + OFF_P);
;         if (tid == 0) *cw = 1 << 30;
;         __syncthreads();
;         if (tid < 256) { float prod = 1.f; int j0 = 0; for (int j = p - 1; j >= 1; --j) { prod *= GTOT[((size_t)j * 4 + h) * DKH + tid]; if (prod < 1e-30f) { j0 = j; break; } }
;             __hip_atomic_fetch_min(cw, j0, __ATOMIC_RELAXED, __HIP_MEMORY_SCOPE_WORKGROUP); }
;         __syncthreads();
;         const int p0 = *cw;
;         for (int pj = p0; pj < p; ++pj) {
;             const f32x4* se = SEND + ((((size_t)pj * 4 + h) * 4 + s) * 8 + w) * 16 * 64 + lane; const float* gt = GTOT + ((size_t)pj * 4 + h) * DKH;
; #pragma unroll
;             for (int hf = 0; hf < 2; ++hf) {
;                 f32x4 gg[8], ee[8];
; #pragma unroll
;                 for (int d8 = 0; d8 < 8; ++d8) { const int dt = 8 * hf + d8; gg[d8] = *(const f32x4*)(gt + 16 * dt + 4 * q); ee[d8] = se[dt * 64]; }
;                 asm volatile("" ::: "memory");
; #pragma unroll
;                 for (int d8 = 0; d8 < 8; ++d8) { const int dt = 8 * hf + d8; S[dt] = S[dt] * gg[d8] + ee[d8]; }
;                 asm volatile("" ::: "memory");
;             }
;         }
;         __syncthreads();
;     }
;     write_stage<NQ>(lds, st0, tid);
;     if (CPP > 1) issue_loads<NQ>(st0, QP, KP, VB, BC, tokbase + CHK, h, s, tid, qkoff, voff);
;     if (PASS == 1 && CPP > 2) issue_loads<NQ>(st1, QP, KP, VB, BC, tokbase + 2 * CHK, h, s, tid, qkoff, voff);
;     __syncthreads();
;     const LAS unsigned char* qnat = lds + OFF_Q + r * QS + q * 16;
; template <int PASS>
; __device__ __forceinline__ void ph_gla(Frame& F) {
;     ...
;     for (int u = blockIdx.x; u < 256; u += F.G) {
;         const int idx = u >> 3, s = idx & 3, ph = (u & 7) * 8 + (idx >> 2), p = ph >> 2, h = ph & 3;
;         if (PASS == 1 && p == gla::NPART - 1) continue;
;         gla::unit<PASS>(F.lds, F.tid, F.lane, F.wave, p, h, s, QP, KP, VB, BC, OG, SEND, GTOT, (const bf16*)(KWS + WS_GB), KIN(5), (float*)(KWS + WS_SS), F.tp_t0, F.tp_acc);
.LBB0_316:
	s_setprio 0
	s_cmp_lt_i32 s30, 4
	s_cselect_b64 s[6:7], -1, 0
	s_cmp_gt_i32 s31, 3
	s_cselect_b64 s[8:9], -1, 0
	s_and_b64 s[6:7], s[6:7], s[8:9]
	s_andn2_b64 vcc, exec, s[6:7]
	s_cbranch_vccnz .LBB0_396
	s_cmpk_gt_i32 s2, 0xff
	s_cbranch_scc1 .LBB0_342
	s_add_u32 s8, s36, 0x26800000
	s_addc_u32 s9, s37, 0
	s_add_u32 s10, s36, 0x28800000
	s_waitcnt vmcnt(0)
	v_and_b32_e32 v16, 63, v0
	s_addc_u32 s11, s37, 0
	v_and_b32_e32 v2, 15, v0
	s_movk_i32 s17, 0x210
	v_lshrrev_b32_e32 v13, 1, v16
	s_add_u32 s12, s36, 0x20800000
	v_mad_u32_u24 v2, v2, s17, 0
	v_and_b32_e32 v13, 24, v13
	s_addc_u32 s13, s37, 0
	v_bfe_u32 v3, v0, 2, 2
	v_add3_u32 v219, v2, v13, 32
	v_lshlrev_b32_e32 v2, 3, v16
	s_add_u32 s3, s36, 0x63000000
	v_lshlrev_b32_e32 v4, 3, v0
	v_and_b32_e32 v220, 0x80, v2
	v_or_b32_e32 v2, v13, v3
	s_addc_u32 s35, s37, 0
	v_lshlrev_b32_e32 v1, 5, v0
	v_and_b32_e32 v5, 0xf8, v4
	s_movk_i32 s6, 0x3c00
	s_add_i32 s14, 0, 0x10c00
	v_mul_u32_u24_e32 v3, 0x220, v2
	v_and_b32_e32 v4, 24, v4
	v_and_or_b32 v1, v1, s6, v5
	v_lshlrev_b32_e32 v5, 4, v0
	v_lshlrev_b32_e32 v204, 2, v0
	v_lshrrev_b32_e32 v6, 1, v0
	s_movk_i32 s16, 0x120
	v_add3_u32 v221, 0, v3, v4
	v_mov_b32_e32 v3, s14
	v_mov_b32_e32 v205, 0
	v_and_b32_e32 v203, 0xf0, v5
	v_and_b32_e32 v5, 0x1f0, v5
	v_and_b32_e32 v6, 0x80, v6
	v_or_b32_e32 v7, 0x200, v0
	v_or_b32_e32 v9, 0x600, v0
	v_and_b32_e32 v10, 0x80, v0
	v_mad_u32_u24 v14, v2, s16, v3
	v_lshl_add_u64 v[2:3], s[36:37], 0, v[204:205]
	s_mov_b64 s[16:17], 0x65000000
	v_xad_u32 v5, v5, v6, 0
	v_lshrrev_b32_e32 v6, 5, v0
	v_lshrrev_b32_e32 v8, 5, v7
	v_lshrrev_b32_e32 v9, 5, v9
	v_xad_u32 v10, v203, v10, s14
	v_lshrrev_b32_e32 v11, 4, v0
	v_lshrrev_b32_e32 v7, 4, v7
	v_and_b32_e32 v12, 48, v0
	s_lshl_b32 s14, s33, 5
	v_lshl_add_u64 v[208:209], v[2:3], 0, s[16:17]
	v_add_u32_e32 v2, 0, v204
	v_mul_u32_u24_e32 v6, 0x220, v6
	v_mul_u32_u24_e32 v8, 0x220, v8
	v_mul_u32_u24_e32 v9, 0x220, v9
	v_mul_u32_u24_e32 v11, 0x120, v11
	v_mul_u32_u24_e32 v7, 0x120, v7
	s_movk_i32 s6, 0x100
	v_sub_u32_e32 v13, 0, v220
	v_bitop3_b32 v4, s14, v220, v4 bitop3:0x36
	v_add_u32_e32 v227, 0x17800, v2
	v_add_u32_e32 v2, 0, v12
	v_and_b32_e32 v202, 0x1f0, v0
	v_and_b32_e32 v218, 0x3fc, v204
	s_mov_b32 s15, 0
	v_cmp_gt_u32_e64 s[6:7], s6, v0
	v_lshl_add_u64 v[206:207], s[12:13], 0, v[204:205]
	s_mov_b32 s44, 0x8000
	s_mov_b32 s45, 0x10000
	s_mov_b32 s46, 0x18000
	s_mov_b32 s47, 0x20000
	v_add_u32_e32 v222, v5, v6
	v_add_u32_e32 v223, v5, v8
	v_add_u32_e32 v224, v5, v9
	v_add_u32_e32 v225, v10, v11
	v_add_u32_e32 v226, v10, v7
	s_mov_b32 s48, 0x3fb8aa3b
	s_mov_b32 s49, 0xc2ce8ed0
	s_mov_b32 s50, 0x42b17218
	v_add_u32_e32 v228, v14, v4
	v_add_u32_e32 v229, 0x17800, v2
	v_add_u32_e32 v230, v221, v13
	v_lshlrev_b32_e32 v210, 4, v16
	s_movk_i32 s51, 0x1000
	s_movk_i32 s52, 0x2000
	v_mov_b32_e32 v231, 0x7f800000
	s_mov_b32 s53, s2
	s_branch .LBB0_321

; #define GAS __attribute__((address_space(1)))
; #define LAS __attribute__((address_space(3)))
; #define KIN(i) (*(const float* const __attribute__((address_space(4)))*)(F.ka + 8 * (i)))
; template <int NC>
; __device__ __forceinline__ void rowblock_bf16(Frame& F, const bf16* X, const bf16* WH, const bf16* WL, LAS float* part, LAS float* sqp) {
;     ...
;     const GAS char* xb = (const GAS char*)X; const GAS char* whb = (const GAS char*)WH; const GAS char* wlb = (const GAS char*)WL;
;     const int lr = lane >> 5, lc = lane & 31;
;     const unsigned xo = (unsigned)((8 * w + lr) * D + 8 * lc) * 2u;
;     const unsigned wo = (unsigned)(r * 2048 + w * 32 + 8 * q) * 2u;
;     v4u xa[4], xb2[4]; rb_bf16x8 bh[NC], bl[NC], ha[NC], la[NC], hb[NC], lb[NC];
; __device__ __forceinline__ void ph_router(Frame& F, int layer, const bf16* H) {
;     const bf16* WH = (const bf16*)(KWS + WS_WRH) + (size_t)layer * NLOG * 2048; const bf16* WL = (const bf16*)(KWS + WS_WRL) + (size_t)layer * NLOG * 2048;
;     const float* wn = KIN(10) + layer * D; const float* bg = KIN(12) + layer * NGRP; const float* br = KIN(14) + layer * NE;
;     bf16* HN = (bf16*)(KWS + WS_HN);
;     int* TKE = (int*)(KWS + WS_TKE); int* TKS = (int*)(KWS + WS_TKS); float* TKG = (float*)(KWS + WS_TKG); int* LIST = (int*)(KWS + WS_LIST);
;     unsigned* gcnt = F.ctl + CW_CNT + 2048 * layer;
;     LAS float* part = (LAS float*)(F.lds);
;     LAS float* sqp = (LAS float*)(F.lds + 98304);
;     LAS float* lg = (LAS float*)(F.lds + 98304 + 2048);
;     LAS float* rs = (LAS float*)(F.lds + 98304 + 2048 + 12288);
;     LAS int* sel = (LAS int*)(F.lds + 98304 + 2048 + 12288 + 256);
;     LAS float* selg = (LAS float*)(F.lds + 98304 + 2048 + 12288 + 256 + 1024);
;     static_assert(98304 + 2048 + 12288 + 256 + 1024 + 512 <= RING_BYTES, "router LDS");
;     volatile LAS int* cntl = F.MISC + MI_CNTL; volatile LAS int* basel = F.MISC + MI_BASEL;
;     for (int blk = blockIdx.x; blk < T / 64; blk += F.G) {
.LBB0_566:
	s_setprio 0
	s_cmp_gt_i32 s30, 7
	s_cselect_b64 s[6:7], -1, 0
	s_cmp_lt_i32 s31, 8
	s_cselect_b64 s[8:9], -1, 0
	s_or_b64 s[6:7], s[6:7], s[8:9]
	s_and_b64 vcc, exec, s[6:7]
	s_cbranch_vccnz .LBB0_676
	s_cmpk_gt_i32 s2, 0xff
	s_cbranch_scc1 .LBB0_622
	s_add_u32 s16, s36, 0x600000
	s_addc_u32 s17, s37, 0
	s_add_u32 s18, s36, 0x660000
	s_addc_u32 s19, s37, 0
	s_add_u32 s26, s36, 0x200000
	s_addc_u32 s27, s37, 0
	s_add_u32 s40, s36, 0x220000
	s_addc_u32 s41, s37, 0
	s_add_u32 s42, s36, 0x240000
	s_addc_u32 s43, s37, 0
	s_add_u32 s44, s36, 0x300000
	s_addc_u32 s45, s37, 0
	s_waitcnt vmcnt(0)
	v_lshlrev_b32_e32 v3, 4, v0
	s_and_b32 s52, s71, 0xffffffc0
	v_and_b32_e32 v8, 48, v0
	v_and_b32_e32 v9, 15, v0
	v_and_b32_e32 v7, 0x1f0, v3
	v_or_b32_e32 v3, s52, v8
	v_lshlrev_b32_e32 v10, 12, v9
	v_mov_b32_e32 v197, 0
	v_add_u32_e32 v196, v3, v10
	v_lshl_add_u64 v[198:199], s[16:17], 0, v[196:197]
	v_lshl_add_u64 v[200:201], s[18:19], 0, v[196:197]
	v_add_u32_e32 v196, 0x200, v196
	v_and_b32_e32 v16, 63, v0
	s_mov_b64 s[8:9], 0x10000
	v_lshl_add_u64 v[212:213], s[16:17], 0, v[196:197]
	v_lshl_add_u64 v[214:215], s[18:19], 0, v[196:197]
	s_add_i32 s3, 0, 0x18000
	v_lshlrev_b32_e32 v5, 2, v0
	v_lshrrev_b32_e32 v6, 5, v16
	v_lshl_add_u64 v[204:205], v[198:199], 0, s[8:9]
	v_lshl_add_u64 v[206:207], v[200:201], 0, s[8:9]
	v_lshl_add_u64 v[216:217], v[212:213], 0, s[8:9]
	v_lshl_add_u64 v[218:219], v[214:215], 0, s[8:9]
	s_add_i32 s8, s52, 0
	v_lshl_add_u32 v4, v16, 2, s3
	s_add_i32 s60, 0, 0x22400
	v_lshl_or_b32 v2, s33, 3, v6
	v_add_u32_e32 v12, s8, v8
	s_movk_i32 s8, 0x210
	s_lshl_b32 s53, s33, 8
	v_add_u32_e32 v229, s3, v5
	s_add_i32 s3, 0, 0x1b800
	v_lshl_or_b32 v194, v2, 12, v7
	v_mul_lo_u32 v13, v2, s8
	v_lshrrev_b32_e32 v2, 2, v0
	s_add_u32 s46, s36, 0x260000
	v_and_or_b32 v2, v2, 12, s52
	s_movk_i32 s12, 0xc0
	s_addc_u32 s47, s37, 0
	s_add_i32 s13, 0, 0x18800
	v_mul_lo_u32 v15, v2, s12
	v_mov_b32_e32 v2, s13
	v_mad_u32_u24 v239, v0, s12, v2
	s_add_i32 s12, 0, 0x1bd00
	v_lshl_add_u32 v240, v0, 3, s12
	s_add_i32 s12, 0, 0x22480
	v_lshlrev_b32_e32 v196, 8, v0
	v_add_u32_e32 v238, s13, v5
	v_add_u32_e32 v241, s12, v5
	v_lshl_add_u64 v[2:3], s[28:29], 0, v[196:197]
	s_mov_b64 s[12:13], 0x8000
	s_add_i32 s14, 0, 0x1b900
	v_lshl_add_u64 v[224:225], v[2:3], 0, s[12:13]
	v_lshrrev_b32_e32 v2, 1, v0
	v_and_b32_e32 v3, 1, v0
	s_add_u32 s48, s36, 0x30800000
	s_load_dwordx2 s[22:23], s[0:1], 0x60
	s_load_dwordx2 s[24:25], s[0:1], 0x70
	v_cmp_gt_u32_e64 s[8:9], 16, v16
	v_add_u32_e32 v236, s3, v5
	v_lshlrev_b32_e32 v16, 4, v2
	v_lshlrev_b32_e32 v3, 2, v3
	v_lshl_add_u32 v243, v2, 2, s3
	s_addc_u32 s49, s37, 0
	s_ashr_i32 s3, s2, 31
	v_add3_u32 v242, s14, v16, v3
	s_lshl_b64 s[14:15], s[2:3], 18
	s_lshl_b32 s3, s33, 15
	v_lshlrev_b32_e32 v2, 12, v6
	v_or3_b32 v196, s3, v2, v7
	s_add_u32 s14, s36, s14
	v_add_u32_e32 v2, s52, v10
	s_mov_b64 s[10:11], 0x20000
	v_add_u32_e32 v11, 0, v7
	v_mul_u32_u24_e32 v14, 0x210, v9
	v_lshl_add_u32 v9, v9, 2, 0
	v_add_u32_e32 v237, 0, v5
	s_movk_i32 s12, 0x80
	v_sub_u32_e32 v3, 0, v5
	s_addc_u32 s15, s37, s15
	s_ashr_i32 s35, s34, 31
	v_or_b32_e32 v228, v2, v8
	v_mbcnt_lo_u32_b32 v2, -1, 0
	v_cmp_gt_u32_e64 s[6:7], 32, v0
	v_add_u32_e32 v1, s60, v5
	v_mov_b32_e32 v195, v197
	v_lshl_add_u64 v[208:209], v[198:199], 0, s[10:11]
	v_lshl_add_u64 v[210:211], v[200:201], 0, s[10:11]
	v_lshl_add_u64 v[220:221], v[212:213], 0, s[10:11]
	v_lshl_add_u64 v[222:223], v[214:215], 0, s[10:11]
	v_cmp_gt_u32_e64 s[10:11], 64, v0
	v_add_u32_e32 v253, 0x2000, v238
	v_add_u32_e32 v254, 0x2800, v237
	v_add_u32_e32 v255, 0x14800, v237
	v_add_u32_e32 v202, 0x17800, v237
	v_add_u32_e32 v203, 0x2800, v238
	v_cmp_gt_u32_e64 s[12:13], s12, v0
	v_lshl_add_u64 v[226:227], s[14:15], 0, v[196:197]
	s_lshl_b64 s[50:51], s[34:35], 18
	s_mov_b32 s3, 0xf800000
	s_mov_b32 s35, 0x3fb8aa3b
	s_mov_b32 s61, 0xc2ce8ed0
	s_mov_b32 s62, 0x42b17218
	v_mov_b32_e32 v244, 1
	v_add_u32_e32 v245, v240, v3
	v_add_u32_e32 v246, v11, v13
	v_add_u32_e32 v247, v12, v14
	v_mbcnt_hi_u32_b32 v248, -1, v2
	v_add_u32_e32 v249, v9, v15
	v_add_u32_e32 v250, s53, v4
	v_mov_b32_e32 v251, 0x7f800000
	s_mov_b32 s52, s2
	s_branch .LBB0_570

; #define LAS __attribute__((address_space(3)))
; template <int LAYER>
; __device__ __forceinline__ void moe_block(Frame& F, const int lo, const int hi, const XcdBarrier& bar) {
;     ...
;     if (IN(pb + 2)) {
;         if (split) {
;             if (N_LAUNCHES != 1) moe_meta(F, LAYER);
;             const int nrt = F.MISC[MI_NRT];
;             { pg8::Gemm g{(const bf16*)H1, (const bf16*)(KWS + WS_WGU) + (size_t)LAYER * NE * 1024 * 2048, nrt * 256, 1024, D};
;               pg8::MoeOrder<true> S{nrt, 4, nrt * 4, F.G, (int)blockIdx.x, (size_t)1024 * 2048 * 2, (const volatile LAS int*)F.MISC, (const int*)(KWS + WS_LIST), 1, 2, 3};
;               pg8::EpiGateUp E{(bf16*)(KWS + WS_ACT), (const float*)(KWS + WS_LRS)};
;               pg8::gemm_phase<pg8::EpiGateUp, pg8::MoeOrder<true>, true>(F.lds + RING_OFF, g, S, E); }
;             { pg8::Gemm g{(const bf16*)(KWS + WS_ACT), (const bf16*)(KWS + WS_WDN) + (size_t)LAYER * NE * 2048 * 512, nrt * 256, 2048, FF};
;               pg8::MoeOrder<false> S{nrt, 8, nrt * 8, F.G, (int)blockIdx.x, (size_t)2048 * 512 * 2, (const volatile LAS int*)F.MISC, (const int*)(KWS + WS_LIST), 2, 0, 0};
;               pg8::EpiDown E{(bf16*)(KWS + WS_Y)};
;               pg8::gemm_phase<pg8::EpiDown, pg8::MoeOrder<false>, true>(F.lds + RING_OFF, g, S, E); }
.LBB0_781:
	s_setprio 0
	s_cmp_lt_u32 s33, 4
	s_cbranch_scc1 .Lprio_skip_4
	s_setprio 1

; template <bool FINAL>
; __device__ __forceinline__ void ph_combine(Frame& F, const bf16* H, bf16* Hout, const float* wn) {
;     int tid_ = threadIdx.x; asm volatile("" : "+v"(tid_)); const int lane_ = tid_ & 63;
;     const bf16* Y = (const bf16*)(KWS + WS_Y); const int* TKE = (const int*)(KWS + WS_TKE); const int* TKS = (const int*)(KWS + WS_TKS); const float* TKG = (const float*)(KWS + WS_TKG); float* RSTD = (float*)(KWS + WS_RSTD);
;     const int gw = blockIdx.x * NWAVES + F.wave, NGW = F.G * NWAVES;
;     f32x4 wv[8];
;     if (FINAL) {
; #pragma unroll
;         for (int j = 0; j < 8; ++j) wv[j] = ((const f32x4*)wn)[lane_ + 64 * j];
;     }
;     for (int t = gw; t < T; t += NGW) {
;         const int r0 = F.MISC[MI_PSTART + TKE[2 * t]] + TKS[2 * t], r1 = F.MISC[MI_PSTART + TKE[2 * t + 1]] + TKS[2 * t + 1]; const float g0 = TKG[2 * t], g1 = TKG[2 * t + 1];
.LBB0_985:
	s_setprio 0
	s_cmp_gt_i32 s30, 11
	s_cselect_b64 s[10:11], -1, 0
	s_cmp_lt_i32 s31, 12
	s_cselect_b64 s[12:13], -1, 0
	s_or_b64 s[10:11], s[10:11], s[12:13]
	s_and_b64 vcc, exec, s[10:11]
	s_cbranch_vccnz .LBB0_1045
	s_lshl_b32 s3, s2, 3
	s_add_i32 s14, s33, s3
	v_mov_b32_e32 v1, v0
	s_cmpk_gt_i32 s14, 0x3fff
	s_cbranch_scc1 .LBB0_991
	s_waitcnt vmcnt(0)
	v_and_b32_e32 v6, 63, v1
	v_mbcnt_lo_u32_b32 v1, -1, 0
	v_mbcnt_hi_u32_b32 v7, -1, v1
	v_and_b32_e32 v1, 64, v7
	v_add_u32_e32 v8, 64, v1
	v_xor_b32_e32 v1, 1, v7
	v_cmp_lt_i32_e32 vcc, v1, v8
	v_xor_b32_e32 v9, 2, v7
	v_xor_b32_e32 v10, 4, v7
	v_cndmask_b32_e32 v1, v7, v1, vcc
	v_cmp_lt_i32_e32 vcc, v9, v8
	s_add_u32 s3, s36, 0x200000
	s_addc_u32 s35, s37, 0
	v_cndmask_b32_e32 v9, v7, v9, vcc
	v_cmp_lt_i32_e32 vcc, v10, v8
	s_add_u32 s40, s36, 0x220000
	s_addc_u32 s41, s37, 0
	v_cndmask_b32_e32 v10, v7, v10, vcc
	v_lshlrev_b32_e32 v58, 2, v10
	v_xor_b32_e32 v10, 8, v7
	v_cmp_lt_i32_e32 vcc, v10, v8
	s_add_u32 s42, s36, 0x240000
	s_addc_u32 s43, s37, 0
	v_cndmask_b32_e32 v10, v7, v10, vcc
	v_lshlrev_b32_e32 v59, 2, v10
	v_xor_b32_e32 v10, 16, v7
	v_cmp_lt_i32_e32 vcc, v10, v8
	s_ashr_i32 s15, s14, 31
	s_lshl_b32 s16, s34, 3
	v_cndmask_b32_e32 v10, v7, v10, vcc
	v_lshlrev_b32_e32 v60, 2, v10
	v_xor_b32_e32 v10, 32, v7
	s_lshl_b64 s[12:13], s[14:15], 2
	v_lshlrev_b32_e32 v2, 3, v6
	v_mov_b32_e32 v3, 0
	v_cmp_lt_i32_e32 vcc, v10, v8
	s_add_u32 s44, s12, 0x260000
	v_lshl_add_u64 v[4:5], s[36:37], 0, v[2:3]
	s_mov_b64 s[10:11], 0x59000000
	v_cndmask_b32_e32 v7, v7, v10, vcc
	s_addc_u32 s45, s13, 0
	s_lshl_b64 s[12:13], s[14:15], 12
	v_lshl_add_u64 v[4:5], v[4:5], 0, s[10:11]
	v_lshlrev_b32_e32 v61, 2, v7
	v_cmp_eq_u32_e64 s[10:11], 0, v6
	s_ashr_i32 s17, s16, 31
	v_or_b32_e32 v6, s12, v2
	v_mov_b32_e32 v7, s13
	s_lshl_b32 s12, s2, 4
	s_lshl_b32 s13, s33, 1
	v_lshlrev_b32_e32 v1, 2, v1
	v_lshlrev_b32_e32 v9, 2, v9
	s_lshl_b64 s[18:19], s[16:17], 2
	s_lshl_b64 s[22:23], s[16:17], 12
	s_add_i32 s24, s12, s13
	s_lshl_b32 s15, s34, 4
	s_add_i32 s17, 0, 0x22000
	s_mov_b32 s46, 0x3c800000
	s_movk_i32 s47, 0x7fff
	s_mov_b32 s48, 0x44800000
	v_mov_b32_e32 v62, 0x358637bd
	s_mov_b32 s49, 0xf800000
	v_mov_b32_e32 v63, 0x260
	v_mov_b32_e32 v64, 1
	s_branch .LBB0_989

; #define KIN(i) (*(const float* const __attribute__((address_space(4)))*)(F.ka + 8 * (i)))
; __device__ __forceinline__ void ph_conv(Frame& F) {
;     const bf16* BG = (const bf16*)(KWS + WS_VB); const bf16* U = (const bf16*)(KWS + WS_GB); bf16* OG = (bf16*)(KWS + WS_OG); const float* cw = KIN(8);
;     const int c = (F.tid & 255) * 8, rh = F.tid >> 8;
;     const f32x4 wa0 = *(const f32x4*)(cw + c), wa1 = *(const f32x4*)(cw + c + 4), wb0 = *(const f32x4*)(cw + D + c), wb1 = *(const f32x4*)(cw + D + c + 4), wc0 = *(const f32x4*)(cw + 2 * D + c), wc1 = *(const f32x4*)(cw + 2 * D + c + 4);
;     for (int blk = blockIdx.x; blk < T / 64; blk += F.G) {
;         const int t0 = blk * 64 + rh * 32;
;         const v4u zero = {0u, 0u, 0u, 0u};
;         v4u p2 = t0 >= 2 ? *(const v4u*)(U + (size_t)(t0 - 2) * D + c) : zero, p1 = t0 >= 1 ? *(const v4u*)(U + (size_t)(t0 - 1) * D + c) : zero;
.LBB0_1120:
	s_setprio 0
	s_cmp_lt_i32 s30, 14
	s_cselect_b64 s[10:11], -1, 0
	s_cmp_gt_i32 s31, 13
	s_cselect_b64 s[14:15], -1, 0
	s_and_b64 s[10:11], s[10:11], s[14:15]
	s_andn2_b64 vcc, exec, s[10:11]
	s_cbranch_vccnz .LBB0_1184
	s_cmpk_gt_i32 s2, 0xff
	s_cbranch_scc1 .LBB0_1130
	s_load_dwordx2 s[10:11], s[0:1], 0x40
	v_lshlrev_b32_e32 v1, 3, v0
	s_waitcnt vmcnt(0)
	v_and_b32_e32 v26, 0x7f8, v1
	v_mov_b32_e32 v35, 0
	v_lshlrev_b32_e32 v34, 2, v26
	s_waitcnt lgkmcnt(0)
	v_lshl_add_u64 v[10:11], s[10:11], 0, v[34:35]
	s_movk_i32 s3, 0x2000
	v_add_co_u32_e32 v32, vcc, s3, v10
	s_mov_b64 s[14:15], 0x2000
	s_nop 0
	v_addc_co_u32_e32 v33, vcc, 0, v11, vcc
	s_movk_i32 s3, 0x4000
	v_lshl_add_u64 v[28:29], v[10:11], 0, s[14:15]
	s_mov_b64 s[14:15], 0x4000
	v_add_co_u32_e32 v36, vcc, s3, v10
	v_lshl_add_u64 v[30:31], v[10:11], 0, s[14:15]
	global_load_dwordx4 v[2:5], v34, s[10:11] offset:16
	global_load_dwordx4 v[6:9], v34, s[10:11]
	v_addc_co_u32_e32 v37, vcc, 0, v11, vcc
	global_load_dwordx4 v[10:13], v[32:33], off
	global_load_dwordx4 v[14:17], v[36:37], off
	global_load_dwordx4 v[18:21], v[28:29], off offset:16
	global_load_dwordx4 v[22:25], v[30:31], off offset:16
	s_add_u32 s10, s36, 0x28800000
	s_addc_u32 s11, s37, 0
	s_add_u32 s14, s36, 0x2c800000
	s_addc_u32 s15, s37, 0
	v_lshlrev_b32_e32 v28, 1, v26
	v_mov_b32_e32 v29, v35
	v_lshrrev_b32_e32 v1, 3, v0
	v_lshl_add_u64 v[36:37], s[14:15], 0, v[28:29]
	v_and_b32_e32 v1, 32, v1
	v_lshl_add_u64 v[28:29], s[36:37], 0, v[28:29]
	s_mov_b64 s[16:17], 0x38800000
	v_lshl_add_u64 v[38:39], v[28:29], 0, s[16:17]
	v_lshl_or_b32 v64, s2, 6, v1
	s_lshl_b32 s3, s34, 6
	s_mov_b32 s18, 0xffff0000
	v_lshlrev_b32_e32 v65, 1, v26
	s_movk_i32 s19, 0x7fff
	s_mov_b32 s22, s2

; #define GAS __attribute__((address_space(1)))
; #define LAS __attribute__((address_space(3)))
; #define KIN(i) (*(const float* const __attribute__((address_space(4)))*)(F.ka + 8 * (i)))
; template <int NC>
; __device__ __forceinline__ void rowblock_bf16(Frame& F, const bf16* X, const bf16* WH, const bf16* WL, LAS float* part, LAS float* sqp) {
;     ...
;     const GAS char* xb = (const GAS char*)X; const GAS char* whb = (const GAS char*)WH; const GAS char* wlb = (const GAS char*)WL;
;     const int lr = lane >> 5, lc = lane & 31;
;     const unsigned xo = (unsigned)((8 * w + lr) * D + 8 * lc) * 2u;
;     const unsigned wo = (unsigned)(r * 2048 + w * 32 + 8 * q) * 2u;
;     v4u xa[4], xb2[4]; rb_bf16x8 bh[NC], bl[NC], ha[NC], la[NC], hb[NC], lb[NC];
; __device__ __forceinline__ void ph_router(Frame& F, int layer, const bf16* H) {
;     const bf16* WH = (const bf16*)(KWS + WS_WRH) + (size_t)layer * NLOG * 2048; const bf16* WL = (const bf16*)(KWS + WS_WRL) + (size_t)layer * NLOG * 2048;
;     const float* wn = KIN(10) + layer * D; const float* bg = KIN(12) + layer * NGRP; const float* br = KIN(14) + layer * NE;
;     bf16* HN = (bf16*)(KWS + WS_HN);
;     int* TKE = (int*)(KWS + WS_TKE); int* TKS = (int*)(KWS + WS_TKS); float* TKG = (float*)(KWS + WS_TKG); int* LIST = (int*)(KWS + WS_LIST);
;     unsigned* gcnt = F.ctl + CW_CNT + 2048 * layer;
;     LAS float* part = (LAS float*)(F.lds);
;     LAS float* sqp = (LAS float*)(F.lds + 98304);
;     LAS float* lg = (LAS float*)(F.lds + 98304 + 2048);
;     LAS float* rs = (LAS float*)(F.lds + 98304 + 2048 + 12288);
;     LAS int* sel = (LAS int*)(F.lds + 98304 + 2048 + 12288 + 256);
;     LAS float* selg = (LAS float*)(F.lds + 98304 + 2048 + 12288 + 256 + 1024);
;     static_assert(98304 + 2048 + 12288 + 256 + 1024 + 512 <= RING_BYTES, "router LDS");
;     volatile LAS int* cntl = F.MISC + MI_CNTL; volatile LAS int* basel = F.MISC + MI_BASEL;
;     for (int blk = blockIdx.x; blk < T / 64; blk += F.G) {
.LBB0_1259:
	s_setprio 0
	s_cmp_gt_i32 s30, 15
	s_cselect_b64 s[10:11], -1, 0
	s_cmp_lt_i32 s31, 16
	s_cselect_b64 s[12:13], -1, 0
	s_or_b64 s[10:11], s[10:11], s[12:13]
	s_and_b64 vcc, exec, s[10:11]
	s_cbranch_vccnz .LBB0_1369
	s_cmpk_gt_i32 s2, 0xff
	s_cbranch_scc1 .LBB0_1315
	s_add_u32 s22, s36, 0x630000
	s_addc_u32 s23, s37, 0
	s_add_u32 s24, s36, 0x690000
	s_addc_u32 s25, s37, 0
	s_add_u32 s42, s36, 0x200000
	s_addc_u32 s43, s37, 0
	s_add_u32 s44, s36, 0x220000
	s_addc_u32 s45, s37, 0
	s_add_u32 s46, s36, 0x240000
	s_addc_u32 s47, s37, 0
	s_add_u32 s48, s36, 0x300000
	s_addc_u32 s49, s37, 0
	s_waitcnt vmcnt(0)
	v_lshlrev_b32_e32 v3, 4, v0
	s_andn2_b32 s71, s71, 63
	s_waitcnt lgkmcnt(0)
	v_and_b32_e32 v8, 48, v0
	v_and_b32_e32 v9, 15, v0
	v_and_b32_e32 v7, 0x1f0, v3
	v_or_b32_e32 v3, s71, v8
	v_lshlrev_b32_e32 v10, 12, v9
	v_mov_b32_e32 v197, 0
	v_add_u32_e32 v196, v3, v10
	v_lshl_add_u64 v[198:199], s[22:23], 0, v[196:197]
	v_lshl_add_u64 v[200:201], s[24:25], 0, v[196:197]
	v_add_u32_e32 v196, 0x200, v196
	v_and_b32_e32 v16, 63, v0
	s_mov_b64 s[12:13], 0x10000
	v_lshl_add_u64 v[212:213], s[22:23], 0, v[196:197]
	v_lshl_add_u64 v[214:215], s[24:25], 0, v[196:197]
	s_add_i32 s3, 0, 0x18000
	v_lshlrev_b32_e32 v5, 2, v0
	v_lshrrev_b32_e32 v6, 5, v16
	v_lshl_add_u64 v[204:205], v[198:199], 0, s[12:13]
	v_lshl_add_u64 v[206:207], v[200:201], 0, s[12:13]
	v_lshl_add_u64 v[216:217], v[212:213], 0, s[12:13]
	v_lshl_add_u64 v[218:219], v[214:215], 0, s[12:13]
	s_add_i32 s12, s71, 0
	v_lshl_add_u32 v4, v16, 2, s3
	s_add_i32 s64, 0, 0x22400
	v_lshl_or_b32 v2, s33, 3, v6
	v_add_u32_e32 v12, s12, v8
	s_movk_i32 s12, 0x210
	s_lshl_b32 s56, s33, 8
	v_add_u32_e32 v229, s3, v5
	s_add_i32 s3, 0, 0x1b800
	v_lshl_or_b32 v194, v2, 12, v7
	v_mul_lo_u32 v13, v2, s12
	v_lshrrev_b32_e32 v2, 2, v0
	s_add_u32 s50, s36, 0x260000
	v_and_or_b32 v2, v2, 12, s71
	s_movk_i32 s16, 0xc0
	s_addc_u32 s51, s37, 0
	s_add_i32 s17, 0, 0x18800
	v_mul_lo_u32 v15, v2, s16
	v_mov_b32_e32 v2, s17
	v_mad_u32_u24 v239, v0, s16, v2
	s_add_i32 s16, 0, 0x1bd00
	v_lshl_add_u32 v240, v0, 3, s16
	s_add_i32 s16, 0, 0x22480
	v_lshlrev_b32_e32 v196, 8, v0
	v_add_u32_e32 v238, s17, v5
	v_add_u32_e32 v241, s16, v5
	v_lshl_add_u64 v[2:3], s[28:29], 0, v[196:197]
	s_mov_b64 s[16:17], 0xa000
	s_add_i32 s18, 0, 0x1b900
	v_lshl_add_u64 v[224:225], v[2:3], 0, s[16:17]
	v_lshrrev_b32_e32 v2, 1, v0
	v_and_b32_e32 v3, 1, v0
	s_add_u32 s52, s36, 0x30800000
	s_load_dwordx2 s[26:27], s[0:1], 0x60
	s_load_dwordx2 s[40:41], s[0:1], 0x70
	v_cmp_gt_u32_e64 s[12:13], 16, v16
	v_add_u32_e32 v236, s3, v5
	v_lshlrev_b32_e32 v16, 4, v2
	v_lshlrev_b32_e32 v3, 2, v3
	v_lshl_add_u32 v243, v2, 2, s3
	s_addc_u32 s53, s37, 0
	s_ashr_i32 s3, s2, 31
	v_add3_u32 v242, s18, v16, v3
	s_lshl_b64 s[18:19], s[2:3], 18
	s_lshl_b32 s3, s33, 15
	v_lshlrev_b32_e32 v2, 12, v6
	v_or3_b32 v196, s3, v2, v7
	s_add_u32 s18, s36, s18
	v_add_u32_e32 v2, s71, v10
	s_mov_b64 s[14:15], 0x20000
	v_add_u32_e32 v11, 0, v7
	v_mul_u32_u24_e32 v14, 0x210, v9
	v_lshl_add_u32 v9, v9, 2, 0
	v_add_u32_e32 v237, 0, v5
	s_movk_i32 s16, 0x80
	v_sub_u32_e32 v3, 0, v5
	s_addc_u32 s19, s37, s19
	s_ashr_i32 s35, s34, 31
	v_or_b32_e32 v228, v2, v8
	v_mbcnt_lo_u32_b32 v2, -1, 0
	v_cmp_gt_u32_e64 s[10:11], 32, v0
	v_add_u32_e32 v1, s64, v5
	v_mov_b32_e32 v195, v197
	v_lshl_add_u64 v[208:209], v[198:199], 0, s[14:15]
	v_lshl_add_u64 v[210:211], v[200:201], 0, s[14:15]
	v_lshl_add_u64 v[220:221], v[212:213], 0, s[14:15]
	v_lshl_add_u64 v[222:223], v[214:215], 0, s[14:15]
	v_cmp_gt_u32_e64 s[14:15], 64, v0
	v_add_u32_e32 v253, 0x2000, v238
	v_add_u32_e32 v254, 0x2800, v237
	v_add_u32_e32 v255, 0x14800, v237
	v_add_u32_e32 v202, 0x17800, v237
	v_add_u32_e32 v203, 0x2800, v238
	v_cmp_gt_u32_e64 s[16:17], s16, v0
	v_lshl_add_u64 v[226:227], s[18:19], 0, v[196:197]
	s_lshl_b64 s[54:55], s[34:35], 18
	s_mov_b32 s3, 0xf800000
	s_mov_b32 s35, 0x3fb8aa3b
	s_mov_b32 s65, 0xc2ce8ed0
	s_mov_b32 s66, 0x42b17218
	v_mov_b32_e32 v244, 1
	v_add_u32_e32 v245, v240, v3
	v_add_u32_e32 v246, v11, v13
	v_add_u32_e32 v247, v12, v14
	v_mbcnt_hi_u32_b32 v248, -1, v2
	v_add_u32_e32 v249, v9, v15
	v_add_u32_e32 v250, s56, v4
	v_mov_b32_e32 v251, 0x7f800000
	s_mov_b32 s56, s2
	s_branch .LBB0_1263

; template <bool FINAL>
; __device__ __forceinline__ void ph_combine(Frame& F, const bf16* H, bf16* Hout, const float* wn) {
;     int tid_ = threadIdx.x; asm volatile("" : "+v"(tid_)); const int lane_ = tid_ & 63;
;     const bf16* Y = (const bf16*)(KWS + WS_Y); const int* TKE = (const int*)(KWS + WS_TKE); const int* TKS = (const int*)(KWS + WS_TKS); const float* TKG = (const float*)(KWS + WS_TKG); float* RSTD = (float*)(KWS + WS_RSTD);
;     const int gw = blockIdx.x * NWAVES + F.wave, NGW = F.G * NWAVES;
;     f32x4 wv[8];
;     if (FINAL) {
; #pragma unroll
;         for (int j = 0; j < 8; ++j) wv[j] = ((const f32x4*)wn)[lane_ + 64 * j];
;     }
;     for (int t = gw; t < T; t += NGW) {
;         const int r0 = F.MISC[MI_PSTART + TKE[2 * t]] + TKS[2 * t], r1 = F.MISC[MI_PSTART + TKE[2 * t + 1]] + TKS[2 * t + 1]; const float g0 = TKG[2 * t], g1 = TKG[2 * t + 1];
.LBB0_1678:
	s_setprio 0
	s_cmp_gt_i32 s30, 19
	s_cselect_b64 s[4:5], -1, 0
	s_cmp_lt_i32 s31, 20
	s_cselect_b64 s[6:7], -1, 0
	s_or_b64 s[4:5], s[4:5], s[6:7]
	s_and_b64 vcc, exec, s[4:5]
	s_cbranch_vccnz .LBB0_1682
	s_lshl_b32 s3, s2, 3
	s_add_i32 s8, s33, s3
	s_cmpk_gt_i32 s8, 0x3fff
	s_cbranch_scc1 .LBB0_1682
	s_load_dwordx4 s[4:7], s[0:1], 0x88
	s_waitcnt vmcnt(0)
	v_and_b32_e32 v36, 63, v0
	v_mov_b32_e32 v33, 0
	v_lshlrev_b32_e32 v32, 4, v36
	v_lshlrev_b32_e32 v38, 3, v36
	s_waitcnt lgkmcnt(0)
	v_lshl_add_u64 v[16:17], s[4:5], 0, v[32:33]
	v_add_co_u32_e32 v34, vcc, 0x1000, v16
	global_load_dwordx4 v[0:3], v32, s[4:5]
	global_load_dwordx4 v[4:7], v32, s[4:5] offset:1024
	global_load_dwordx4 v[8:11], v32, s[4:5] offset:2048
	global_load_dwordx4 v[12:15], v32, s[4:5] offset:3072
	v_addc_co_u32_e32 v35, vcc, 0, v17, vcc
	global_load_dwordx4 v[16:19], v[34:35], off
	global_load_dwordx4 v[20:23], v[34:35], off offset:1024
	global_load_dwordx4 v[24:27], v[34:35], off offset:2048
	global_load_dwordx4 v[28:31], v[34:35], off offset:3072
	v_mbcnt_lo_u32_b32 v36, -1, 0
	v_mbcnt_hi_u32_b32 v36, -1, v36
	v_and_b32_e32 v37, 64, v36
	v_add_u32_e32 v37, 64, v37
	v_xor_b32_e32 v40, 1, v36
	v_cmp_lt_i32_e32 vcc, v40, v37
	s_add_u32 s18, s36, 0x220000
	s_addc_u32 s19, s37, 0
	v_cndmask_b32_e32 v40, v36, v40, vcc
	v_lshlrev_b32_e32 v42, 2, v40
	v_xor_b32_e32 v40, 2, v36
	v_cmp_lt_i32_e32 vcc, v40, v37
	s_add_u32 s20, s36, 0x200000
	s_addc_u32 s21, s37, 0
	v_cndmask_b32_e32 v40, v36, v40, vcc
	v_lshlrev_b32_e32 v43, 2, v40
	v_xor_b32_e32 v40, 4, v36
	v_cmp_lt_i32_e32 vcc, v40, v37
	s_add_u32 s22, s36, 0x240000
	v_mov_b32_e32 v39, v33
	v_cndmask_b32_e32 v40, v36, v40, vcc
	v_lshlrev_b32_e32 v44, 2, v40
	v_xor_b32_e32 v40, 8, v36
	v_cmp_lt_i32_e32 vcc, v40, v37
	s_addc_u32 s23, s37, 0
	v_lshl_add_u64 v[34:35], s[36:37], 0, v[38:39]
	v_cndmask_b32_e32 v40, v36, v40, vcc
	v_lshlrev_b32_e32 v45, 2, v40
	v_xor_b32_e32 v40, 16, v36
	v_cmp_lt_i32_e32 vcc, v40, v37
	s_mov_b64 s[0:1], 0x59000000
	s_ashr_i32 s9, s8, 31
	v_cndmask_b32_e32 v40, v36, v40, vcc
	s_lshl_b32 s4, s34, 3
	v_lshl_add_u64 v[34:35], v[34:35], 0, s[0:1]
	v_lshlrev_b32_e32 v46, 2, v40
	v_xor_b32_e32 v40, 32, v36
	s_lshl_b64 s[0:1], s[8:9], 13
	v_cmp_lt_i32_e32 vcc, v40, v37
	s_add_u32 s0, s6, s0
	s_addc_u32 s1, s7, s1
	v_cndmask_b32_e32 v36, v36, v40, vcc
	v_lshlrev_b32_e32 v47, 2, v36
	v_lshl_add_u64 v[36:37], s[0:1], 0, v[32:33]
	s_mov_b64 s[0:1], 0x1000
	v_lshl_add_u64 v[36:37], v[36:37], 0, s[0:1]
	s_ashr_i32 s5, s4, 31
	s_lshl_b32 s0, s2, 4
	s_lshl_b32 s1, s33, 1
	s_lshl_b64 s[6:7], s[4:5], 13
	s_add_i32 s2, s0, s1
	s_lshl_b32 s24, s34, 4
	s_lshl_b64 s[0:1], s[8:9], 12
	s_add_u32 s0, s36, s0
	s_addc_u32 s1, s37, s1
	v_lshl_add_u64 v[38:39], s[0:1], 0, v[38:39]
	s_mov_b64 s[0:1], 0x3c800e00
	v_lshl_add_u64 v[38:39], v[38:39], 0, s[0:1]
	s_lshl_b64 s[10:11], s[4:5], 12
	s_add_i32 s5, 0, 0x22000
	v_mov_b32_e32 v32, 0x358637bd
	s_mov_b32 s9, 0xf800000
	v_mov_b32_e32 v48, 0x260
